# speedup vs baseline: 1.0134x; 1.0134x over previous
.LBB0_2:
	s_or_b64 exec, exec, s[6:7]
	v_bfe_u32 v16, v0, 6, 1
	v_lshl_or_b32 v2, v16, 4, v19
	s_movk_i32 s6, 0x80
	v_and_or_b32 v3, v0, s6, v18
	v_lshlrev_b32_e32 v6, 2, v2
	v_mad_u32_u24 v12, v2, s8, v3
	v_or_b32_e32 v2, 0x10a00, v6
	v_or_b32_e32 v6, 0x10a20, v6
	v_add_u32_e32 v14, 0x800, v12
	v_lshlrev_b32_e32 v50, 2, v0
	v_and_b32_e32 v50, 0x200, v50
	v_lshl_add_u32 v50, s2, 1, v50
	v_or_b32_e32 v50, v50, v16
	v_ashrrev_i32_e32 v51, 31, v50
	v_lshlrev_b64 v[50:51], 10, v[50:51]
	v_lshl_add_u64 v[50:51], s[12:13], 0, v[50:51]
	v_lshl_add_u64 v[50:51], v[50:51], 0, v[20:21]
	v_lshlrev_b32_e32 v40, 1, v0
	v_bfe_u32 v41, v0, 3, 1
	v_and_b32_e32 v40, 8, v40
	v_and_b32_e32 v42, 16, v0
	v_and_or_b32 v43, v0, 3, v40
	v_lshlrev_b32_e32 v40, 2, v41
	v_or3_b32 v43, v43, v40, v42
	v_lshlrev_b32_e32 v43, 2, v43
	v_or_b32_e32 v44, 0x10a80, v43
	v_or_b32_e32 v45, 0x10a00, v43
	v_lshl_or_b32 v46, v41, 3, s3
	v_or3_b32 v46, v46, v42, v1
	v_ashrrev_i32_e32 v47, 31, v46
	v_lshlrev_b64 v[46:47], 1, v[46:47]
	v_lshl_add_u64 v[48:49], s[14:15], 0, v[46:47]
	v_lshl_add_u64 v[46:47], s[16:17], 0, v[46:47]
	v_cmp_gt_u32_e32 vcc, 32, v0
	s_waitcnt lgkmcnt(0)
	s_barrier
	ds_read2_b32 v[10:11], v12 offset1:68
	ds_read_b128 v[2:5], v2
	ds_read_b128 v[6:9], v6
	ds_read2_b32 v[52:53], v12 offset0:136 offset1:204
	ds_read2_b32 v[12:13], v14 offset0:32 offset1:100
	ds_read2_b32 v[14:15], v14 offset0:168 offset1:236
	ds_read_b32 v44, v44
	ds_read_b32 v45, v45
	s_waitcnt lgkmcnt(6)
	v_pk_mul_f32 v[2:3], v[10:11], v[2:3]
	s_waitcnt lgkmcnt(4)
	v_pk_mul_f32 v[4:5], v[52:53], v[4:5]
	v_cvt_pk_f16_f32 v2, v2, v3
	v_cvt_pk_f16_f32 v3, v4, v5
	s_waitcnt lgkmcnt(3)
	v_pk_mul_f32 v[4:5], v[12:13], v[6:7]
	s_waitcnt lgkmcnt(2)
	v_pk_mul_f32 v[6:7], v[14:15], v[8:9]
	v_cvt_pk_f16_f32 v4, v4, v5
	v_cvt_pk_f16_f32 v5, v6, v7
	global_store_dwordx4 v[50:51], v[2:5], off sc0 sc1
	s_and_saveexec_b64 s[4:5], vcc
	s_cbranch_execz .LBB0_4
	s_waitcnt lgkmcnt(0)
	v_cvt_f16_f32_e32 v44, v44
	v_cvt_f16_f32_e32 v45, v45
	global_store_short v[48:49], v44, off sc1
	global_store_short v[46:47], v45, off sc1
